# k_fused prologue: issue actF/tri loads before mask wait, counted vmcnt in PROJ0
# speedup vs baseline: 1.0016x; 1.0016x over previous
_Z7k_fusedPKDF16_S0_S0_S0_PKfS2_S2_Pf:
	v_lshrrev_b32_e32 v222, 6, v0
	v_and_b32_e32 v1, 63, v0
	s_load_dwordx8 s[24:31], s[0:1], 0x8
	s_load_dwordx4 s[36:39], s[0:1], 0x28
	v_lshlrev_b32_e32 v4, 2, v222
	v_lshlrev_b32_e32 v5, 3, v1
	v_lshl_or_b32 v2, v222, 11, v5
	v_lshlrev_b32_e32 v224, 12, v222
	v_or_b32_e32 v6, 1, v4
	v_lshlrev_b32_e32 v223, 1, v2
	v_readfirstlane_b32 s3, v224
	v_lshl_or_b32 v2, v6, 9, v5
	v_lshlrev_b32_e32 v225, 10, v6
	v_mov_b32_e32 v211, 0
	s_mov_b32 m0, s3
	v_lshlrev_b32_e32 v210, 1, v2
	v_readfirstlane_b32 s3, v225
	s_waitcnt lgkmcnt(0)
	global_load_lds_dwordx4 v223, s[24:25]
	v_lshl_add_u64 v[2:3], s[24:25], 0, v[210:211]
	s_mov_b32 m0, s3
	v_or_b32_e32 v6, 2, v4
	global_load_lds_dwordx4 v[2:3], off
	v_lshl_or_b32 v2, v6, 9, v5
	v_lshlrev_b32_e32 v212, 1, v2
	v_mov_b32_e32 v213, v211
	v_lshl_add_u64 v[2:3], s[24:25], 0, v[212:213]
	v_lshlrev_b32_e32 v213, 10, v6
	v_or_b32_e32 v4, 3, v4
	v_readfirstlane_b32 s3, v213
	s_mov_b32 m0, s3
	v_mov_b32_e32 v215, v211
	global_load_lds_dwordx4 v[2:3], off
	v_lshl_or_b32 v2, v4, 9, v5
	v_lshlrev_b32_e32 v214, 1, v2
	v_lshl_add_u64 v[2:3], s[24:25], 0, v[214:215]
	v_lshlrev_b32_e32 v215, 10, v4
	s_nop 0
	v_readfirstlane_b32 s3, v215
	s_mov_b32 m0, s3
	s_movk_i32 s3, 0xff
	global_load_lds_dwordx4 v[2:3], off
	v_and_b32_e32 v2, 0x7f, v0
	v_lshlrev_b32_e32 v2, 2, v2
	global_load_dword v4, v2, s[36:37]
	global_load_dword v5, v2, s[38:39]
	s_lshl_b32 s3, s2, 8
	s_load_dwordx2 s[4:5], s[0:1], 0x0
	v_and_b32_e32 v6, 0xff, v0
	v_or_b32_e32 v6, s3, v6
	v_ashrrev_i32_e32 v7, 31, v6
	v_lshl_add_u64 v[6:7], v[6:7], 2, s[30:31]
	global_load_dword v244, v[6:7], off
	v_mov_b32_e32 v208, s3
	v_lshl_or_b32 v2, s2, 3, v222
	v_ashrrev_i32_e32 v3, 31, v2
	v_lshlrev_b64 v[2:3], 13, v[2:3]
	s_waitcnt lgkmcnt(0)
	v_lshl_add_u64 v[6:7], s[4:5], 0, v[2:3]
	v_mov_b32_e32 v2, 0
	v_lshlrev_b32_e32 v206, 4, v1
	v_mov_b32_e32 v207, v2
	v_lshl_add_u64 v[6:7], v[6:7], 0, v[206:207]
	v_lshlrev_b32_e32 v211, 13, v222
	v_ashrrev_i32_e32 v209, 31, v208
	v_lshl_add_u64 v[8:9], v[208:209], 2, s[30:31]
	v_or_b32_e32 v3, v211, v206
	v_lshl_add_u64 v[8:9], v[8:9], 0, v[206:207]
	global_load_dwordx4 v[68:71], v[8:9], off
	global_load_dwordx4 v[130:133], v[6:7], off
	global_load_dwordx4 v[134:137], v[6:7], off offset:1024
	global_load_dwordx4 v[138:141], v[6:7], off offset:2048
	global_load_dwordx4 v[142:145], v[6:7], off offset:3072
	s_movk_i32 s33, 0x1000
	v_add_co_u32_e32 v14, vcc, s33, v6
	s_nop 1
	v_addc_co_u32_e32 v15, vcc, 0, v7, vcc
	global_load_dwordx4 v[146:149], v[14:15], off
	global_load_dwordx4 v[150:153], v[14:15], off offset:1024
	global_load_dwordx4 v[154:157], v[14:15], off offset:2048
	global_load_dwordx4 v[158:161], v[14:15], off offset:3072
	v_lshlrev_b32_e32 v10, 1, v3
	global_load_dwordx4 v[186:189], v10, s[28:29] offset:16
	global_load_dwordx4 v[190:193], v10, s[28:29]
	global_load_dwordx4 v[178:181], v10, s[28:29] offset:2064
	global_load_dwordx4 v[182:185], v10, s[28:29] offset:2048
	v_mov_b32_e32 v11, v2
	v_lshl_add_u64 v[8:9], s[28:29], 0, v[10:11]
	v_add_co_u32_e32 v12, vcc, s33, v8
	s_mov_b64 s[34:35], 0x1000
	s_nop 0
	v_addc_co_u32_e32 v13, vcc, 0, v9, vcc
	s_mov_b64 s[40:41], 0x1800
	v_lshl_add_u64 v[10:11], v[8:9], 0, s[34:35]
	v_lshl_add_u64 v[8:9], v[8:9], 0, s[40:41]
	global_load_dwordx4 v[170:173], v[12:13], off
	global_load_dwordx4 v[174:177], v[10:11], off offset:16
	global_load_dwordx4 v[162:165], v[12:13], off offset:2048
	global_load_dwordx4 v[166:169], v[8:9], off offset:16
	s_waitcnt vmcnt(17)
	v_cmp_gt_u32_e32 vcc, 0x100, v0
	s_and_saveexec_b64 s[4:5], vcc
	v_lshlrev_b32_e32 v12, 4, v0
	v_and_b32_e32 v13, 0xe3, v0
	v_lshlrev_b32_e32 v14, 1, v0
	v_and_b32_e32 v12, 64, v12
	s_mov_b32 s8, 0x20000
	v_and_b32_e32 v14, 48, v14
	v_lshl_or_b32 v13, v13, 2, v12
	v_or3_b32 v13, v13, v14, s8
	v_add_f32_e32 v12, -1.0, v244
	v_mul_f32_e32 v12, 0x47000000, v12
	v_mul_f32_e32 v12, 0x3fb8aa3b, v12
	ds_write_b32 v13, v12
	s_or_b64 exec, exec, s[4:5]
	s_waitcnt lgkmcnt(0)
	s_barrier
	ds_read_b128 v[4:7], v206 offset:8192
	ds_read_b128 v[72:75], v206 offset:9216
	s_load_dwordx2 s[30:31], s[0:1], 0x38
	s_mov_b32 s0, 0x47000000
	s_mov_b32 s42, 0x3fb8aa3b
	s_mov_b32 s43, 0xff800000
	v_lshrrev_b32_e32 v96, 5, v1
	v_lshlrev_b32_e32 v97, 4, v96
	v_lshl_or_b32 v209, v222, 11, v206
	v_lshlrev_b32_e32 v1, 5, v1
	s_add_u32 s54, s24, 0x8000
	v_lshlrev_b32_e32 v207, 2, v96
	s_addc_u32 s55, s25, 0
	v_or_b32_e32 v227, 0x10000, v3
	s_mov_b32 s56, 0xc1d00000
	s_mov_b64 s[44:45], 0x20000
	s_mov_b64 s[46:47], 0x20800
	s_mov_b64 s[48:49], 0x21000
	s_mov_b32 s57, 0x21000
	s_mov_b64 s[50:51], 0x21800
	v_mov_b32_e32 v194, 0x3c003c00
	s_waitcnt lgkmcnt(0)
	s_waitcnt vmcnt(15)
	v_mfma_f32_32x32x16_f16 v[36:51], v[4:7], v[130:133], 0
	ds_read_b128 v[4:7], v206
	ds_read_b128 v[76:79], v206 offset:1024
	ds_read_b128 v[20:23], v206 offset:24576
	ds_read_b128 v[80:83], v206 offset:25600
	ds_read_b128 v[52:55], v206 offset:16384
	ds_read_b128 v[84:87], v206 offset:17408
	v_max_f32_e32 v71, v71, v71
	s_waitcnt lgkmcnt(1)
	v_mfma_f32_32x32x16_f16 v[52:67], v[130:133], v[52:55], 0
	v_max_f32_e32 v70, v70, v70
	v_max_f32_e32 v70, v70, v71
	s_waitcnt vmcnt(14)
	v_mfma_f32_32x32x16_f16 v[36:51], v[72:75], v[134:137], v[36:51]
	s_waitcnt lgkmcnt(0)
	v_mfma_f32_32x32x16_f16 v[52:67], v[134:137], v[84:87], v[52:67]
	ds_read_b128 v[72:75], v206 offset:10240
	ds_read_b128 v[84:87], v206 offset:11264
	s_waitcnt lgkmcnt(1)
	s_waitcnt vmcnt(13)
	v_mfma_f32_32x32x16_f16 v[36:51], v[72:75], v[138:141], v[36:51]
	ds_read_b128 v[72:75], v206 offset:18432
	ds_read_b128 v[88:91], v206 offset:19456
	s_waitcnt lgkmcnt(1)
	v_mfma_f32_32x32x16_f16 v[52:67], v[138:141], v[72:75], v[52:67]
	ds_read_b128 v[72:75], v206 offset:12288
	s_waitcnt vmcnt(12)
	v_mfma_f32_32x32x16_f16 v[36:51], v[84:87], v[142:145], v[36:51]
	v_mbcnt_lo_u32_b32 v84, -1, 0
	v_mbcnt_hi_u32_b32 v92, -1, v84
	ds_read_b128 v[84:87], v206 offset:13312
	v_xor_b32_e32 v93, 1, v92
	v_xor_b32_e32 v94, 2, v92
	v_xor_b32_e32 v95, 4, v92
	s_waitcnt lgkmcnt(2)
	v_mfma_f32_32x32x16_f16 v[52:67], v[142:145], v[88:91], v[52:67]
	v_and_b32_e32 v88, 64, v92
	v_add_u32_e32 v98, 64, v88
	v_cmp_lt_i32_e32 vcc, v93, v98
	ds_read_b128 v[88:91], v206 offset:21504
	s_waitcnt lgkmcnt(2)
	s_waitcnt vmcnt(11)
	v_mfma_f32_32x32x16_f16 v[36:51], v[72:75], v[146:149], v[36:51]
	ds_read_b128 v[72:75], v206 offset:20480
	s_waitcnt lgkmcnt(0)
	v_mfma_f32_32x32x16_f16 v[52:67], v[146:149], v[72:75], v[52:67]
	v_cndmask_b32_e32 v72, v92, v93, vcc
	v_lshlrev_b32_e32 v72, 2, v72
	v_max3_f32 v73, v68, v69, v70
	ds_bpermute_b32 v72, v72, v73
	v_cmp_lt_i32_e32 vcc, v94, v98
	s_waitcnt lgkmcnt(0)
	v_max_f32_e32 v72, v72, v72
	v_cndmask_b32_e32 v68, v92, v94, vcc
	v_lshlrev_b32_e32 v74, 2, v68
	ds_read_b128 v[68:71], v206 offset:14336
	s_waitcnt vmcnt(10)
	v_mfma_f32_32x32x16_f16 v[36:51], v[84:87], v[150:153], v[36:51]
	v_max_f32_e32 v84, v73, v72
	ds_bpermute_b32 v85, v74, v84
	v_cmp_lt_i32_e32 vcc, v95, v98
	s_waitcnt lgkmcnt(0)
	v_max_f32_e32 v85, v85, v85
	v_mfma_f32_32x32x16_f16 v[52:67], v[150:153], v[88:91], v[52:67]
	v_cndmask_b32_e32 v72, v92, v95, vcc
	v_lshlrev_b32_e32 v86, 2, v72
	v_max_f32_e32 v92, v84, v85
	ds_read_b128 v[72:75], v206 offset:15360
	ds_bpermute_b32 v93, v86, v92
	s_waitcnt lgkmcnt(0)
	v_max_f32_e32 v93, v93, v93
	s_waitcnt vmcnt(9)
	v_mfma_f32_32x32x16_f16 v[36:51], v[68:71], v[154:157], v[36:51]
	ds_read_b128 v[68:71], v206 offset:22528
	ds_read_b128 v[84:87], v206 offset:23552
	v_max_f32_e32 v92, v92, v93
	global_load_dwordx4 v[88:91], v97, s[36:37]
	v_readlane_b32 s3, v92, 0
	v_readlane_b32 s2, v92, 8
	v_readlane_b32 s5, v92, 16
	v_readlane_b32 s4, v92, 24
	s_waitcnt lgkmcnt(1)
	v_mfma_f32_32x32x16_f16 v[52:67], v[154:157], v[68:71], v[52:67]
	v_add_f32_e64 v68, s2, -1.0
	v_add_f32_e64 v69, s3, -1.0
	v_readlane_b32 s7, v92, 32
	v_readlane_b32 s6, v92, 40
	v_add_f32_e64 v70, s4, -1.0
	v_add_f32_e64 v71, s5, -1.0
	v_pk_mul_f32 v[68:69], v[68:69], s[0:1] op_sel_hi:[1,0]
	v_readlane_b32 s9, v92, 48
	v_readlane_b32 s8, v92, 56
	v_mfma_f32_32x32x16_f16 v[20:35], v[20:23], v[130:133], 0
	v_mul_f32_e64 v70, v70, s0
	v_mul_f32_e64 v71, v71, s0
	v_mul_f32_e64 v92, v68, s42
	v_mul_f32_e64 v93, v69, s42
	v_mul_f32_e64 v94, v70, s42
	v_mul_f32_e64 v95, v71, s42
	v_max3_f32 v68, v93, s43, v92
	v_max3_f32 v68, v68, v95, v94
	s_waitcnt vmcnt(9)
	v_mfma_f32_32x32x16_f16 v[36:51], v[72:75], v[158:161], v[36:51]
	v_add_f32_e64 v72, s6, -1.0
	v_add_f32_e64 v73, s7, -1.0
	v_mul_f32_e64 v72, v72, s0
	v_mul_f32_e64 v73, v73, s0
	s_waitcnt lgkmcnt(0)
	v_mfma_f32_32x32x16_f16 v[52:67], v[158:161], v[84:87], v[52:67]
	v_mul_f32_e64 v84, v72, s42
	v_mul_f32_e64 v85, v73, s42
	v_add_f32_e64 v86, s8, -1.0
	v_add_f32_e64 v87, s9, -1.0
	v_max3_f32 v98, v68, v85, v84
	ds_read_b128 v[68:71], v206 offset:26624
	v_cvt_pk_f16_f32 v43, v42, v43
	v_cvt_pk_f16_f32 v42, v40, v41
	v_cvt_pk_f16_f32 v41, v38, v39
	v_mfma_f32_32x32x16_f16 v[20:35], v[80:83], v[134:137], v[20:35]
	v_mul_f32_e64 v80, v86, s0
	v_mul_f32_e64 v81, v87, s0
	v_cvt_pk_f16_f32 v40, v36, v37
	v_mul_f32_e64 v86, v80, s42
	v_mul_f32_e64 v87, v81, s42
	global_load_dwordx4 v[72:75], v97, s[36:37] offset:32
	v_max3_f32 v80, v98, v87, v86
	v_add_f32_e32 v98, 0xc53b8000, v80
	ds_read_b128 v[80:83], v206 offset:27648
	global_load_dwordx4 v[36:39], v97, s[36:37] offset:64
	ds_write_b128 v209, v[40:43] offset:32768
	v_cvt_pk_f16_f32 v43, v50, v51
	v_cvt_pk_f16_f32 v40, v44, v45
	v_cvt_pk_f16_f32 v44, v52, v53
	global_load_dwordx4 v[50:53], v97, s[36:37] offset:96
	s_waitcnt lgkmcnt(2)
	v_mfma_f32_32x32x16_f16 v[20:35], v[68:71], v[138:141], v[20:35]
	ds_read_b128 v[68:71], v206 offset:28672
	v_cvt_pk_f16_f32 v42, v48, v49
	v_cvt_pk_f16_f32 v41, v46, v47
	ds_write_b128 v209, v[40:43] offset:33792
	ds_read_b128 v[40:43], v206 offset:30720
	v_cvt_pk_f16_f32 v47, v58, v59
	v_cvt_pk_f16_f32 v46, v56, v57
	s_waitcnt lgkmcnt(4)
	v_mfma_f32_32x32x16_f16 v[20:35], v[80:83], v[142:145], v[20:35]
	ds_read_b128 v[80:83], v206 offset:29696
	v_cvt_pk_f16_f32 v45, v54, v55
	ds_write_b128 v209, v[44:47] offset:49152
	v_cvt_pk_f16_f32 v45, v66, v67
	ds_read_b128 v[46:49], v206 offset:31744
	v_cvt_pk_f16_f32 v44, v64, v65
	v_cmp_ge_f32_e64 s[0:1], v92, v98
	s_waitcnt lgkmcnt(5)
	v_mfma_f32_32x32x16_f16 v[20:35], v[68:71], v[146:149], v[20:35]
	v_cmp_ge_f32_e64 s[2:3], v93, v98
	v_cmp_ge_f32_e64 s[4:5], v94, v98
	v_cmp_ge_f32_e64 s[6:7], v95, v98
	v_cmp_ge_f32_e64 s[8:9], v84, v98
	v_cmp_ge_f32_e64 s[10:11], v85, v98
	v_cmp_ge_f32_e64 s[12:13], v86, v98
	v_cmp_ge_f32_e64 s[14:15], v87, v98
	v_mfma_f32_32x32x16_f16 v[4:19], v[4:7], v[130:133], 0
	s_waitcnt lgkmcnt(2)
	v_mfma_f32_32x32x16_f16 v[20:35], v[80:83], v[150:153], v[20:35]
	v_mfma_f32_32x32x16_f16 v[4:19], v[76:79], v[134:137], v[4:19]
	v_mfma_f32_32x32x16_f16 v[20:35], v[40:43], v[154:157], v[20:35]
	v_cvt_pk_f16_f32 v43, v62, v63
	v_cvt_pk_f16_f32 v42, v60, v61
	ds_write_b128 v209, v[42:45] offset:50176
	ds_read_b128 v[40:43], v206 offset:2048
	ds_read_b128 v[54:57], v206 offset:3072
	s_waitcnt lgkmcnt(1)
	v_mfma_f32_32x32x16_f16 v[4:19], v[40:43], v[138:141], v[4:19]
	s_waitcnt lgkmcnt(0)
	v_mfma_f32_32x32x16_f16 v[4:19], v[54:57], v[142:145], v[4:19]
	v_mfma_f32_32x32x16_f16 v[20:35], v[46:49], v[158:161], v[20:35]
	ds_read_b128 v[44:47], v206 offset:4096
	ds_read_b128 v[58:61], v206 offset:5120
	ds_read_b128 v[62:65], v206 offset:6144
	ds_read_b128 v[66:69], v206 offset:7168
	s_waitcnt lgkmcnt(0)
	s_barrier
	s_waitcnt vmcnt(3)
	s_nop 4
	v_add_f32_e32 v20, v20, v88
	v_mfma_f32_32x32x16_f16 v[4:19], v[44:47], v[146:149], v[4:19]
	v_add_f32_e32 v21, v89, v21
	v_add_f32_e32 v22, v90, v22
	v_add_f32_e32 v23, v91, v23
	s_waitcnt vmcnt(2)
	v_add_f32_e32 v24, v24, v72
	v_add_f32_e32 v25, v73, v25
	v_add_f32_e32 v26, v74, v26
	v_add_f32_e32 v27, v75, v27
	v_mfma_f32_32x32x16_f16 v[4:19], v[58:61], v[150:153], v[4:19]
	s_waitcnt vmcnt(1)
	v_add_f32_e32 v28, v28, v36
	v_add_f32_e32 v29, v37, v29
	v_add_f32_e32 v30, v38, v30
	v_add_f32_e32 v31, v39, v31
	s_waitcnt vmcnt(0)
	v_add_f32_e32 v32, v32, v50
	v_add_f32_e32 v33, v51, v33
	v_add_f32_e32 v34, v52, v34
	v_mfma_f32_32x32x16_f16 v[4:19], v[62:65], v[154:157], v[4:19]
	v_add_f32_e32 v35, v53, v35
	v_mul_f32_e32 v20, 0xbfb8aa3b, v20
	v_mul_f32_e32 v21, 0xbfb8aa3b, v21
	v_mul_f32_e32 v22, 0xbfb8aa3b, v22
	v_mul_f32_e32 v23, 0xbfb8aa3b, v23
	v_mul_f32_e32 v24, 0xbfb8aa3b, v24
	v_mul_f32_e32 v25, 0xbfb8aa3b, v25
	v_mfma_f32_32x32x16_f16 v[4:19], v[66:69], v[158:161], v[4:19]
	v_mul_f32_e32 v26, 0xbfb8aa3b, v26
	v_mul_f32_e32 v27, 0xbfb8aa3b, v27
	v_mul_f32_e32 v28, 0xbfb8aa3b, v28
	v_mul_f32_e32 v29, 0xbfb8aa3b, v29
	v_mul_f32_e32 v30, 0xbfb8aa3b, v30
	v_mul_f32_e32 v31, 0xbfb8aa3b, v31
	v_mul_f32_e32 v32, 0xbfb8aa3b, v32
	v_mul_f32_e32 v33, 0xbfb8aa3b, v33
	v_mul_f32_e32 v34, 0xbfb8aa3b, v34
	v_mul_f32_e32 v35, 0xbfb8aa3b, v35
	v_exp_f32_e32 v20, v20
	v_exp_f32_e32 v21, v21
	v_exp_f32_e32 v22, v22
	v_exp_f32_e32 v23, v23
	v_exp_f32_e32 v24, v24
	v_exp_f32_e32 v25, v25
	v_exp_f32_e32 v26, v26
	v_exp_f32_e32 v27, v27
	v_exp_f32_e32 v28, v28
	v_exp_f32_e32 v29, v29
	v_exp_f32_e32 v30, v30
	v_exp_f32_e32 v31, v31
	v_exp_f32_e32 v32, v32
	v_exp_f32_e32 v33, v33
	v_exp_f32_e32 v34, v34
	v_exp_f32_e32 v35, v35
	v_add_f32_e32 v20, 1.0, v20
	v_add_f32_e32 v21, 1.0, v21
	v_add_f32_e32 v22, 1.0, v22
	v_add_f32_e32 v23, 1.0, v23
	v_add_f32_e32 v24, 1.0, v24
	v_add_f32_e32 v25, 1.0, v25
	v_add_f32_e32 v26, 1.0, v26
	v_add_f32_e32 v27, 1.0, v27
	v_add_f32_e32 v28, 1.0, v28
	v_add_f32_e32 v29, 1.0, v29
	v_add_f32_e32 v30, 1.0, v30
	v_add_f32_e32 v31, 1.0, v31
	v_add_f32_e32 v32, 1.0, v32
	v_add_f32_e32 v33, 1.0, v33
	v_add_f32_e32 v34, 1.0, v34
	v_add_f32_e32 v35, 1.0, v35
	v_rcp_f32_e32 v20, v20
	v_rcp_f32_e32 v21, v21
	v_rcp_f32_e32 v22, v22
	v_rcp_f32_e32 v23, v23
	v_rcp_f32_e32 v24, v24
	v_rcp_f32_e32 v25, v25
	v_rcp_f32_e32 v26, v26
	v_rcp_f32_e32 v27, v27
	v_rcp_f32_e32 v28, v28
	v_rcp_f32_e32 v29, v29
	v_rcp_f32_e32 v30, v30
	v_rcp_f32_e32 v31, v31
	v_rcp_f32_e32 v32, v32
	v_rcp_f32_e32 v33, v33
	v_rcp_f32_e32 v34, v34
	v_rcp_f32_e32 v35, v35
	v_cvt_pk_f16_f32 v198, v4, v5
	v_lshl_or_b32 v4, v222, 14, v1
	v_mov_b32_e32 v5, v2
	v_lshl_add_u64 v[216:217], s[28:29], 0, v[4:5]
	v_or_b32_e32 v4, 0x2000, v4
	v_lshrrev_b32_e32 v1, 1, v0
	v_lshl_add_u64 v[218:219], s[28:29], 0, v[4:5]
	v_and_b32_e32 v4, 16, v1
	v_mov_b32_e32 v36, 0x20000
	v_lshl_add_u64 v[4:5], s[36:37], 0, v[4:5]
	s_mov_b64 s[28:29], 0x80
	v_lshl_or_b32 v226, v96, 6, v36
	v_cvt_pk_f16_f32 v199, v6, v7
	v_cvt_pk_f16_f32 v200, v8, v9
	v_cvt_pk_f16_f32 v201, v10, v11
	v_cvt_pk_f16_f32 v202, v12, v13
	v_cvt_pk_f16_f32 v203, v14, v15
	v_cvt_pk_f16_f32 v204, v16, v17
	v_cvt_pk_f16_f32 v205, v18, v19
	v_cvt_pk_f16_f32 v229, v20, v21
	v_cvt_pk_f16_f32 v230, v22, v23
	v_cvt_pk_f16_f32 v232, v24, v25
	v_cvt_pk_f16_f32 v234, v26, v27
	v_cvt_pk_f16_f32 v228, v28, v29
	v_cvt_pk_f16_f32 v231, v30, v31
	v_cvt_pk_f16_f32 v233, v32, v33
	v_cvt_pk_f16_f32 v235, v34, v35
	v_lshl_add_u64 v[220:221], v[4:5], 0, s[28:29]
	s_mov_b64 s[36:37], 0
	s_branch .LBB1_6

	.amdhsa_kernel _Z7k_fusedPKDF16_S0_S0_S0_PKfS2_S2_Pf
		.amdhsa_group_segment_fixed_size 132096
		.amdhsa_private_segment_fixed_size 0
		.amdhsa_kernarg_size 64
		.amdhsa_user_sgpr_count 2
		.amdhsa_user_sgpr_dispatch_ptr 0
		.amdhsa_user_sgpr_queue_ptr 0
		.amdhsa_user_sgpr_kernarg_segment_ptr 1
		.amdhsa_user_sgpr_dispatch_id 0
		.amdhsa_user_sgpr_kernarg_preload_length 0
		.amdhsa_user_sgpr_kernarg_preload_offset 0
		.amdhsa_user_sgpr_private_segment_size 0
		.amdhsa_uses_dynamic_stack 0
		.amdhsa_enable_private_segment 0
		.amdhsa_system_sgpr_workgroup_id_x 1
		.amdhsa_system_sgpr_workgroup_id_y 0
		.amdhsa_system_sgpr_workgroup_id_z 0
		.amdhsa_system_sgpr_workgroup_info 0
		.amdhsa_system_vgpr_workitem_id 0
		.amdhsa_next_free_vgpr 248
		.amdhsa_next_free_sgpr 96
		.amdhsa_accum_offset 248
		.amdhsa_reserve_vcc 1
		.amdhsa_float_round_mode_32 0
		.amdhsa_float_round_mode_16_64 0
		.amdhsa_float_denorm_mode_32 3
		.amdhsa_float_denorm_mode_16_64 3
		.amdhsa_dx10_clamp 1
		.amdhsa_ieee_mode 1
		.amdhsa_fp16_overflow 0
		.amdhsa_tg_split 0
		.amdhsa_exception_fp_ieee_invalid_op 0
		.amdhsa_exception_fp_denorm_src 0
		.amdhsa_exception_fp_ieee_div_zero 0
		.amdhsa_exception_fp_ieee_overflow 0
		.amdhsa_exception_fp_ieee_underflow 0
		.amdhsa_exception_fp_ieee_inexact 0
		.amdhsa_exception_int_div_zero 0
	.end_amdhsa_kernel

amdhsa.kernels:
  - .agpr_count:     16
    .args:
      - .actual_access:  read_only
        .address_space:  global
        .offset:         0
        .size:           8
        .value_kind:     global_buffer
      - .actual_access:  read_only
        .address_space:  global
        .offset:         8
        .size:           8
        .value_kind:     global_buffer
      - .actual_access:  read_only
        .address_space:  global
        .offset:         16
        .size:           8
        .value_kind:     global_buffer
      - .actual_access:  read_only
        .address_space:  global
        .offset:         24
        .size:           8
        .value_kind:     global_buffer
      - .actual_access:  write_only
        .address_space:  global
        .offset:         32
        .size:           8
        .value_kind:     global_buffer
      - .actual_access:  write_only
        .address_space:  global
        .offset:         40
        .size:           8
        .value_kind:     global_buffer
      - .actual_access:  read_only
        .address_space:  global
        .offset:         48
        .size:           8
        .value_kind:     global_buffer
      - .actual_access:  read_only
        .address_space:  global
        .offset:         56
        .size:           8
        .value_kind:     global_buffer
      - .actual_access:  read_only
        .address_space:  global
        .offset:         64
        .size:           8
        .value_kind:     global_buffer
      - .actual_access:  read_only
        .address_space:  global
        .offset:         72
        .size:           8
        .value_kind:     global_buffer
      - .actual_access:  read_only
        .address_space:  global
        .offset:         80
        .size:           8
        .value_kind:     global_buffer
      - .actual_access:  write_only
        .address_space:  global
        .offset:         88
        .size:           8
        .value_kind:     global_buffer
      - .actual_access:  write_only
        .address_space:  global
        .offset:         96
        .size:           8
        .value_kind:     global_buffer
    .group_segment_fixed_size: 40960
    .kernarg_segment_align: 8
    .kernarg_segment_size: 104
    .language:       OpenCL C
    .language_version:
      - 2
      - 0
    .max_flat_workgroup_size: 256
    .name:           _Z5k_triPKfS0_S0_S0_PDF16_S1_S0_S0_S0_S0_S0_S1_S1_
    .private_segment_fixed_size: 0
    .sgpr_count:     33
    .sgpr_spill_count: 0
    .symbol:         _Z5k_triPKfS0_S0_S0_PDF16_S1_S0_S0_S0_S0_S0_S1_S1_.kd
    .uniform_work_group_size: 1
    .uses_dynamic_stack: false
    .vgpr_count:     248
    .vgpr_spill_count: 0
    .wavefront_size: 64
  - .agpr_count:     0
    .args:
      - .actual_access:  read_only
        .address_space:  global
        .offset:         0
        .size:           8
        .value_kind:     global_buffer
      - .address_space:  global
        .offset:         8
        .size:           8
        .value_kind:     global_buffer
      - .address_space:  global
        .offset:         16
        .size:           8
        .value_kind:     global_buffer
      - .actual_access:  read_only
        .address_space:  global
        .offset:         24
        .size:           8
        .value_kind:     global_buffer
      - .actual_access:  read_only
        .address_space:  global
        .offset:         32
        .size:           8
        .value_kind:     global_buffer
      - .actual_access:  read_only
        .address_space:  global
        .offset:         40
        .size:           8
        .value_kind:     global_buffer
      - .actual_access:  read_only
        .address_space:  global
        .offset:         48
        .size:           8
        .value_kind:     global_buffer
      - .actual_access:  write_only
        .address_space:  global
        .offset:         56
        .size:           8
        .value_kind:     global_buffer
    .group_segment_fixed_size: 132096
    .kernarg_segment_align: 8
    .kernarg_segment_size: 64
    .language:       OpenCL C
    .language_version:
      - 2
      - 0
    .max_flat_workgroup_size: 512
    .name:           _Z7k_fusedPKDF16_S0_S0_S0_PKfS2_S2_Pf
    .private_segment_fixed_size: 0
    .sgpr_count:     64
    .sgpr_spill_count: 0
    .symbol:         _Z7k_fusedPKDF16_S0_S0_S0_PKfS2_S2_Pf.kd
    .uniform_work_group_size: 1
    .uses_dynamic_stack: false
    .vgpr_count:     248
    .vgpr_spill_count: 0
    .wavefront_size: 64
